# T3a stage F: forward substitution of the 16x16 diagonal blocks in right-looking form (batched ds_read_b128, independent FMAs per step, same summation order)
# speedup vs baseline: 1.0003x; 1.0003x over previous
; __device__ __forceinline__ void phase1(const int WID_, const In& I, char* lds) {
;     ...
;         if (wv == 0) {
;             const int d = lane >> 4, cc = lane & 15;
;             const float* nb = NMF + (d >> 1) * 1024 + (16 * (d & 1)) * 32 + 16 * (d & 1);
;             float T[16];
; #pragma unroll
;             for (int i = 0; i < 16; ++i) {
;                 float acc = (i == cc) ? 1.f : 0.f;
; #pragma unroll
;                 for (int j4 = 0; j4 < i; j4 += 4) { const float4 n4 = *(const float4*)(nb + i * 32 + j4);
;                     acc += n4.x * T[j4]; if (j4 + 1 < i) acc += n4.y * T[j4 + 1]; if (j4 + 2 < i) acc += n4.z * T[j4 + 2]; if (j4 + 3 < i) acc += n4.w * T[j4 + 3]; }
;                 T[i] = acc;
.LBB0_1446:
	v_and_b32_e32 v80, 15, v58
	s_andn2_b64 vcc, exec, s[0:1]
	v_lshlrev_b32_e32 v10, 1, v80
	v_mul_u32_u24_e32 v59, 0x50, v78
	s_cbranch_vccnz .LBB0_1448
	v_lshlrev_b32_e32 v60, 7, v58
	v_and_b32_e32 v60, 0xfffff000, v60
	v_and_b32_e32 v61, 16, v58
	v_add_u32_e32 v60, s77, v60
	v_lshlrev_b32_e32 v74, 7, v61
	v_lshlrev_b32_e32 v75, 2, v61
	v_add3_u32 v81, v60, v74, v75
	ds_read_b128 v[86:89], v81 offset:128
	ds_read_b128 v[90:93], v81 offset:256
	ds_read_b128 v[94:97], v81 offset:384
	ds_read_b128 v[98:101], v81 offset:512
	ds_read_b128 v[102:105], v81 offset:640
	ds_read_b128 v[106:109], v81 offset:768
	ds_read_b128 v[110:113], v81 offset:896
	ds_read_b128 v[114:117], v81 offset:1024
	ds_read_b128 v[118:121], v81 offset:1152
	ds_read_b128 v[122:125], v81 offset:1280
	ds_read_b128 v[126:129], v81 offset:1408
	ds_read_b128 v[130:133], v81 offset:1536
	ds_read_b128 v[134:137], v81 offset:1664
	ds_read_b128 v[138:141], v81 offset:1792
	ds_read_b128 v[142:145], v81 offset:1920
	v_cmp_eq_u32_e32 vcc, 0, v80
	v_cmp_eq_u32_e64 s[98:99], 1, v80
	v_cmp_eq_u32_e64 s[100:101], 2, v80
	v_cndmask_b32_e64 v0, 0, 1.0, vcc
	v_cmp_eq_u32_e32 vcc, 3, v80
	v_cndmask_b32_e64 v1, 0, 1.0, s[98:99]
	v_cmp_eq_u32_e64 s[98:99], 4, v80
	v_cndmask_b32_e64 v2, 0, 1.0, s[100:101]
	v_cmp_eq_u32_e64 s[100:101], 5, v80
	v_cndmask_b32_e64 v3, 0, 1.0, vcc
	v_cmp_eq_u32_e32 vcc, 6, v80
	v_cndmask_b32_e64 v4, 0, 1.0, s[98:99]
	v_cmp_eq_u32_e64 s[98:99], 7, v80
	v_cndmask_b32_e64 v5, 0, 1.0, s[100:101]
	v_cmp_eq_u32_e64 s[100:101], 8, v80
	v_cndmask_b32_e64 v6, 0, 1.0, vcc
	v_cmp_eq_u32_e32 vcc, 9, v80
	v_cndmask_b32_e64 v7, 0, 1.0, s[98:99]
	v_cmp_eq_u32_e64 s[98:99], 10, v80
	v_cndmask_b32_e64 v8, 0, 1.0, s[100:101]
	v_cmp_eq_u32_e64 s[100:101], 11, v80
	v_cndmask_b32_e64 v9, 0, 1.0, vcc
	v_cmp_eq_u32_e32 vcc, 12, v80
	v_cndmask_b32_e64 v11, 0, 1.0, s[98:99]
	v_cmp_eq_u32_e64 s[98:99], 13, v80
	v_cndmask_b32_e64 v12, 0, 1.0, s[100:101]
	v_cmp_eq_u32_e64 s[100:101], 14, v80
	v_cndmask_b32_e64 v13, 0, 1.0, vcc
	v_cmp_eq_u32_e32 vcc, 15, v80
	v_cndmask_b32_e64 v14, 0, 1.0, s[98:99]
	v_cndmask_b32_e64 v15, 0, 1.0, s[100:101]
	v_cndmask_b32_e64 v68, 0, 1.0, vcc
	s_waitcnt lgkmcnt(14)
	v_fmac_f32_e32 v1, v86, v0
	s_waitcnt lgkmcnt(13)
	v_fmac_f32_e32 v2, v90, v0
	s_waitcnt lgkmcnt(12)
	v_fmac_f32_e32 v3, v94, v0
	s_waitcnt lgkmcnt(11)
	v_fmac_f32_e32 v4, v98, v0
	s_waitcnt lgkmcnt(10)
	v_fmac_f32_e32 v5, v102, v0
	s_waitcnt lgkmcnt(9)
	v_fmac_f32_e32 v6, v106, v0
	s_waitcnt lgkmcnt(8)
	v_fmac_f32_e32 v7, v110, v0
	s_waitcnt lgkmcnt(7)
	v_fmac_f32_e32 v8, v114, v0
	s_waitcnt lgkmcnt(6)
	v_fmac_f32_e32 v9, v118, v0
	s_waitcnt lgkmcnt(5)
	v_fmac_f32_e32 v11, v122, v0
	s_waitcnt lgkmcnt(4)
	v_fmac_f32_e32 v12, v126, v0
	s_waitcnt lgkmcnt(3)
	v_fmac_f32_e32 v13, v130, v0
	s_waitcnt lgkmcnt(2)
	v_fmac_f32_e32 v14, v134, v0
	s_waitcnt lgkmcnt(1)
	v_fmac_f32_e32 v15, v138, v0
	s_waitcnt lgkmcnt(0)
	v_fmac_f32_e32 v68, v142, v0
	ds_read_b128 v[146:149], v81 offset:656
	ds_read_b128 v[150:153], v81 offset:784
	ds_read_b128 v[154:157], v81 offset:912
	ds_read_b128 v[158:161], v81 offset:1040
	ds_read_b128 v[162:165], v81 offset:1168
	ds_read_b128 v[166:169], v81 offset:1296
	ds_read_b128 v[170:173], v81 offset:1424
	ds_read_b128 v[60:63], v81 offset:1552
	ds_read_b128 v[64:67], v81 offset:1680
	ds_read_b128 v[70:73], v81 offset:1808
	ds_read_b128 v[82:85], v81 offset:1936
	v_fmac_f32_e32 v2, v91, v1
	v_fmac_f32_e32 v3, v95, v1
	v_fmac_f32_e32 v4, v99, v1
	v_fmac_f32_e32 v5, v103, v1
	v_fmac_f32_e32 v6, v107, v1
	v_fmac_f32_e32 v7, v111, v1
	v_fmac_f32_e32 v8, v115, v1
	v_fmac_f32_e32 v9, v119, v1
	v_fmac_f32_e32 v11, v123, v1
	v_fmac_f32_e32 v12, v127, v1
	v_fmac_f32_e32 v13, v131, v1
	v_fmac_f32_e32 v14, v135, v1
	v_fmac_f32_e32 v15, v139, v1
	v_fmac_f32_e32 v68, v143, v1
	v_fmac_f32_e32 v3, v96, v2
	v_fmac_f32_e32 v4, v100, v2
	v_fmac_f32_e32 v5, v104, v2
	v_fmac_f32_e32 v6, v108, v2
	v_fmac_f32_e32 v7, v112, v2
	v_fmac_f32_e32 v8, v116, v2
	v_fmac_f32_e32 v9, v120, v2
	v_fmac_f32_e32 v11, v124, v2
	v_fmac_f32_e32 v12, v128, v2
	v_fmac_f32_e32 v13, v132, v2
	v_fmac_f32_e32 v14, v136, v2
	v_fmac_f32_e32 v15, v140, v2
	v_fmac_f32_e32 v68, v144, v2
	v_fmac_f32_e32 v4, v101, v3
	v_fmac_f32_e32 v5, v105, v3
	v_fmac_f32_e32 v6, v109, v3
	v_fmac_f32_e32 v7, v113, v3
	v_fmac_f32_e32 v8, v117, v3
	v_fmac_f32_e32 v9, v121, v3
	v_fmac_f32_e32 v11, v125, v3
	v_fmac_f32_e32 v12, v129, v3
	v_fmac_f32_e32 v13, v133, v3
	v_fmac_f32_e32 v14, v137, v3
	v_fmac_f32_e32 v15, v141, v3
	v_fmac_f32_e32 v68, v145, v3
	s_waitcnt lgkmcnt(0)
; __device__ __forceinline__ unsigned pk2(float lo, float hi) { const f32x2h v = {lo, hi}; const bf16x2h b = __builtin_convertvector(v, bf16x2h); return __builtin_bit_cast(unsigned, b); }
; __device__ __forceinline__ bf16 f2bf(float f) { return (bf16)(pk2(f, f) & 0xffffu); }
; __device__ __forceinline__ void phase1(const int WID_, const In& I, char* lds) {
;     ...
;             for (int i = 0; i < 16; ++i) {
;                 float acc = (i == cc) ? 1.f : 0.f;
; #pragma unroll
;                 for (int j4 = 0; j4 < i; j4 += 4) { const float4 n4 = *(const float4*)(nb + i * 32 + j4);
;                     acc += n4.x * T[j4]; if (j4 + 1 < i) acc += n4.y * T[j4 + 1]; if (j4 + 2 < i) acc += n4.z * T[j4 + 2]; if (j4 + 3 < i) acc += n4.w * T[j4 + 3]; }
;                 T[i] = acc;
;             }
;             bf16* tm = MAT(O_TM) + (16 * d) * LD + 16 * d + cc;
; #pragma unroll
;             for (int i = 0; i < 16; ++i) tm[i * LD] = f2bf(T[i]);
;             bf16* tt = MAT(O_TT) + (d >> 1) * 32 * 40 + (16 * (d & 1) + cc) * 40 + 16 * (d & 1);
;             *(uint4*)(tt) = make_uint4(pk2(T[0], T[1]), pk2(T[2], T[3]), pk2(T[4], T[5]), pk2(T[6], T[7]));
;             *(uint4*)(tt + 8) = make_uint4(pk2(T[8], T[9]), pk2(T[10], T[11]), pk2(T[12], T[13]), pk2(T[14], T[15]));
;             { const int blk = lane >> 5, r16 = (lane >> 1) & 15, hf = lane & 1;
;               *(uint4*)(MAT(O_TM) + (32 * blk + r16) * LD + 32 * blk + 16 + 8 * hf) = make_uint4(0, 0, 0, 0);
;               *(uint4*)(MAT(O_TT) + blk * 32 * 40 + (16 + r16) * 40 + 8 * hf) = make_uint4(0, 0, 0, 0); }
	ds_read_b128 v[86:89], v81 offset:1184
	ds_read_b128 v[90:93], v81 offset:1312
	ds_read_b128 v[94:97], v81 offset:1440
	ds_read_b128 v[98:101], v81 offset:1568
	ds_read_b128 v[102:105], v81 offset:1696
	ds_read_b128 v[106:109], v81 offset:1824
	ds_read_b128 v[110:113], v81 offset:1952
	ds_read_b128 v[114:117], v81 offset:1712
	ds_read_b128 v[118:121], v81 offset:1840
	ds_read_b128 v[122:125], v81 offset:1968
	v_fmac_f32_e32 v5, v146, v4
	v_fmac_f32_e32 v6, v150, v4
	v_fmac_f32_e32 v7, v154, v4
	v_fmac_f32_e32 v8, v158, v4
	v_fmac_f32_e32 v9, v162, v4
	v_fmac_f32_e32 v11, v166, v4
	v_fmac_f32_e32 v12, v170, v4
	v_fmac_f32_e32 v13, v60, v4
	v_fmac_f32_e32 v14, v64, v4
	v_fmac_f32_e32 v15, v70, v4
	v_fmac_f32_e32 v68, v82, v4
	v_fmac_f32_e32 v6, v151, v5
	v_fmac_f32_e32 v7, v155, v5
	v_fmac_f32_e32 v8, v159, v5
	v_fmac_f32_e32 v9, v163, v5
	v_fmac_f32_e32 v11, v167, v5
	v_fmac_f32_e32 v12, v171, v5
	v_fmac_f32_e32 v13, v61, v5
	v_fmac_f32_e32 v14, v65, v5
	v_fmac_f32_e32 v15, v71, v5
	v_fmac_f32_e32 v68, v83, v5
	v_fmac_f32_e32 v7, v156, v6
	v_fmac_f32_e32 v8, v160, v6
	v_fmac_f32_e32 v9, v164, v6
	v_fmac_f32_e32 v11, v168, v6
	v_fmac_f32_e32 v12, v172, v6
	v_fmac_f32_e32 v13, v62, v6
	v_fmac_f32_e32 v14, v66, v6
	v_fmac_f32_e32 v15, v72, v6
	v_fmac_f32_e32 v68, v84, v6
	v_fmac_f32_e32 v8, v161, v7
	v_fmac_f32_e32 v9, v165, v7
	v_fmac_f32_e32 v11, v169, v7
	v_fmac_f32_e32 v12, v173, v7
	v_fmac_f32_e32 v13, v63, v7
	v_fmac_f32_e32 v14, v67, v7
	v_fmac_f32_e32 v15, v73, v7
	v_fmac_f32_e32 v68, v85, v7
	s_waitcnt lgkmcnt(0)
	v_fmac_f32_e32 v9, v86, v8
	v_fmac_f32_e32 v11, v90, v8
	v_fmac_f32_e32 v12, v94, v8
	v_fmac_f32_e32 v13, v98, v8
	v_fmac_f32_e32 v14, v102, v8
	v_fmac_f32_e32 v15, v106, v8
	v_fmac_f32_e32 v68, v110, v8
	v_fmac_f32_e32 v11, v91, v9
	v_fmac_f32_e32 v12, v95, v9
	v_fmac_f32_e32 v13, v99, v9
	v_fmac_f32_e32 v14, v103, v9
	v_fmac_f32_e32 v15, v107, v9
	v_fmac_f32_e32 v68, v111, v9
	v_fmac_f32_e32 v12, v96, v11
	v_fmac_f32_e32 v13, v100, v11
	v_fmac_f32_e32 v14, v104, v11
	v_fmac_f32_e32 v15, v108, v11
	v_fmac_f32_e32 v68, v112, v11
	v_fmac_f32_e32 v13, v101, v12
	v_fmac_f32_e32 v14, v105, v12
	v_fmac_f32_e32 v15, v109, v12
	v_fmac_f32_e32 v68, v113, v12
	v_fmac_f32_e32 v14, v114, v13
	v_fmac_f32_e32 v15, v118, v13
	v_fmac_f32_e32 v68, v122, v13
	v_fmac_f32_e32 v15, v119, v14
	v_fmac_f32_e32 v68, v123, v14
	v_fmac_f32_e32 v68, v124, v15
	v_cvt_pk_bf16_f32 v146, v0, v1
	v_cvt_pk_bf16_f32 v147, v2, v3
	v_cvt_pk_bf16_f32 v148, v4, v5
	v_cvt_pk_bf16_f32 v149, v6, v7
	v_cvt_pk_bf16_f32 v150, v8, v9
	v_cvt_pk_bf16_f32 v151, v11, v12
	v_cvt_pk_bf16_f32 v152, v13, v14
	v_cvt_pk_bf16_f32 v153, v15, v68
	v_and_b32_e32 v60, -16, v58
	v_mul_lo_u32 v74, v60, s9
	v_lshlrev_b32_e32 v60, 1, v60
	v_add3_u32 v74, v74, v60, v10
	ds_write_b16 v74, v146
	ds_write_b16_d16_hi v74, v146 offset:144
	ds_write_b16 v74, v147 offset:288
	ds_write_b16_d16_hi v74, v147 offset:432
	ds_write_b16 v74, v148 offset:576
	ds_write_b16_d16_hi v74, v148 offset:720
	ds_write_b16 v74, v149 offset:864
	ds_write_b16_d16_hi v74, v149 offset:1008
	ds_write_b16 v74, v150 offset:1152
	ds_write_b16_d16_hi v74, v150 offset:1296
	ds_write_b16 v74, v151 offset:1440
	ds_write_b16_d16_hi v74, v151 offset:1584
	ds_write_b16 v74, v152 offset:1728
	ds_write_b16_d16_hi v74, v152 offset:1872
	ds_write_b16 v74, v153 offset:2016
	ds_write_b16_d16_hi v74, v153 offset:2160
	v_and_b32_e32 v8, 0xffffffe0, v58
	s_movk_i32 s0, 0x50
	v_mul_lo_u32 v60, v8, s0
	s_add_i32 s0, 0, 0x1f400
	v_add_u32_e32 v11, s0, v60
	v_and_b32_e32 v61, 16, v58
	v_lshlrev_b32_e32 v61, 1, v61
	v_add3_u32 v75, v11, v59, v61
	ds_write_b128 v75, v[146:149]
	ds_write_b128 v75, v[150:153] offset:16
	v_bfe_u32 v0, v58, 1, 4
	v_lshlrev_b32_e32 v6, 3, v58
	v_or_b32_e32 v1, v0, v8
	v_mul_lo_u32 v1, v1, s9
	v_lshlrev_b32_e32 v3, 1, v6
	s_mov_b32 s4, s5
	v_add_u32_e32 v1, 0, v1
	v_lshlrev_b32_e32 v2, 1, v8
	v_and_b32_e32 v3, 16, v3
	s_mov_b32 s6, s5
	s_mov_b32 s7, s5
	v_mov_b64_e32 v[4:5], s[4:5]
	v_mul_u32_u24_e32 v0, 0x50, v0
	v_add3_u32 v1, v1, v2, v3
	v_mov_b64_e32 v[6:7], s[6:7]
	v_add3_u32 v0, v11, v0, v3
	ds_write_b128 v1, v[4:7] offset:32
	ds_write_b128 v0, v[4:7] offset:1280
